# v21
# baseline (speedup 1.0000x reference)
.LBB1_9:
	s_add_i32 s82, s48, 2
	s_and_b32 s28, s82, 2
	s_bitcmp1_b32 s82, 1
	s_cselect_b64 s[4:5], -1, 0
	s_cselect_b32 s83, 1, 0
	s_cmp_eq_u32 s28, 0
	s_cbranch_scc1 .LBB1_14
	ds_read_b128 v[0:3], v225

.LBB1_12:
	s_waitcnt vmcnt(8)
	s_waitcnt lgkmcnt(0)
	s_barrier
	s_setprio 1
	s_waitcnt lgkmcnt(0)
	v_mfma_f32_16x16x32_f16 v[128:131], v[148:151], v[166:169], v[128:131]
	v_mfma_f32_16x16x32_f16 v[128:131], v[152:155], v[174:177], v[128:131]
	v_mfma_f32_16x16x32_f16 v[120:123], v[160:163], v[174:177], v[120:123]
	v_mfma_f32_16x16x32_f16 v[120:123], v[156:159], v[166:169], v[120:123]
	v_mfma_f32_16x16x32_f16 v[104:107], v[156:159], v[170:173], v[104:107]
	v_mfma_f32_16x16x32_f16 v[104:107], v[160:163], v[178:181], v[104:107]
	v_mfma_f32_16x16x32_f16 v[112:115], v[152:155], v[178:181], v[112:115]
	v_mfma_f32_16x16x32_f16 v[112:115], v[148:151], v[170:173], v[112:115]
	v_mfma_f32_16x16x32_f16 v[96:99], v[148:151], v[182:185], v[96:99]
	v_mfma_f32_16x16x32_f16 v[96:99], v[152:155], v[190:193], v[96:99]
	v_mfma_f32_16x16x32_f16 v[88:91], v[160:163], v[190:193], v[88:91]
	v_mfma_f32_16x16x32_f16 v[88:91], v[156:159], v[182:185], v[88:91]
	v_mfma_f32_16x16x32_f16 v[72:75], v[156:159], v[186:189], v[72:75]
	v_mfma_f32_16x16x32_f16 v[72:75], v[160:163], v[214:217], v[72:75]
	v_mfma_f32_16x16x32_f16 v[80:83], v[152:155], v[214:217], v[80:83]
	v_mfma_f32_16x16x32_f16 v[80:83], v[148:151], v[186:189], v[80:83]
	s_setprio 0
	s_setprio 1
	v_mfma_f32_16x16x32_f16 v[124:127], v[132:135], v[166:169], v[124:127]
	v_mfma_f32_16x16x32_f16 v[124:127], v[136:139], v[174:177], v[124:127]
	v_mfma_f32_16x16x32_f16 v[116:119], v[144:147], v[174:177], v[116:119]
	v_mfma_f32_16x16x32_f16 v[116:119], v[140:143], v[166:169], v[116:119]
	v_mfma_f32_16x16x32_f16 v[100:103], v[140:143], v[170:173], v[100:103]
	v_mfma_f32_16x16x32_f16 v[100:103], v[144:147], v[178:181], v[100:103]
	v_mfma_f32_16x16x32_f16 v[108:111], v[136:139], v[178:181], v[108:111]
	v_mfma_f32_16x16x32_f16 v[108:111], v[132:135], v[170:173], v[108:111]
	v_mfma_f32_16x16x32_f16 v[92:95], v[132:135], v[182:185], v[92:95]
	v_mfma_f32_16x16x32_f16 v[92:95], v[136:139], v[190:193], v[92:95]
	v_mfma_f32_16x16x32_f16 v[84:87], v[144:147], v[190:193], v[84:87]
	v_mfma_f32_16x16x32_f16 v[84:87], v[140:143], v[182:185], v[84:87]
	v_mfma_f32_16x16x32_f16 v[68:71], v[140:143], v[186:189], v[68:71]
	v_mfma_f32_16x16x32_f16 v[68:71], v[144:147], v[214:217], v[68:71]
	v_mfma_f32_16x16x32_f16 v[76:79], v[136:139], v[214:217], v[76:79]
	v_mfma_f32_16x16x32_f16 v[76:79], v[132:135], v[186:189], v[76:79]
	s_setprio 0
	s_barrier
	s_add_u32 s28, s44, 0xfff00080
	s_addc_u32 s46, s45, -1
	s_cmp_eq_u32 s48, 60
	s_cselect_b32 s49, s31, s46
	s_cselect_b32 s47, s35, s81
	s_cselect_b32 s46, s78, s80
	s_mov_b32 m0, s52
	s_cselect_b32 s48, s77, s28
	s_add_u32 s50, s46, 0x100000
	ds_read_b128 v[188:191], v226 offset:16384
	ds_read_b128 v[176:179], v226 offset:18432
	ds_read_b128 v[192:195], v227 offset:16384
	ds_read_b128 v[180:183], v227 offset:18432
	ds_read_b128 v[172:175], v226 offset:20480
	ds_read_b128 v[164:167], v226 offset:22528
	ds_read_b128 v[184:187], v227 offset:20480
	ds_read_b128 v[168:171], v227 offset:22528
	global_load_lds_dwordx4 v200, s[46:47]
	s_mov_b32 m0, s53
	s_addc_u32 s51, s47, 0
	global_load_lds_dwordx4 v196, s[46:47]
	s_mov_b32 m0, s55
	s_add_u32 s84, s46, 0x80
	s_addc_u32 s85, s47, 0
	global_load_lds_dwordx4 v200, s[50:51]
	s_mov_b32 m0, s56
	s_add_u32 s86, s48, 0x80
	s_addc_u32 s87, s49, 0
	s_and_b64 s[4:5], exec, s[4:5]
	global_load_lds_dwordx4 v196, s[50:51]
	s_mov_b32 m0, s43
	s_mov_b64 s[50:51], -1
	global_load_lds_dwordx4 v202, s[48:49]
	s_mov_b32 m0, s54
	s_mov_b64 vcc, s[4:5]
	global_load_lds_dwordx4 v198, s[48:49]
	s_cbranch_vccz .LBB1_18
	v_cvt_pkrtz_f16_f32 v0, v0, v1
	v_cvt_pkrtz_f16_f32 v1, v2, v3
	v_add_u32_e32 v0, 0x20002, v0
	v_add_u32_e32 v1, 0x20002, v1
	v_and_b32_e32 v0, 0xfffcfffc, v0
	v_and_b32_e32 v1, 0xfffcfffc, v1
	global_store_dwordx2 v231, v[0:1], s[90:91]
	s_waitcnt vmcnt(9)
	s_mov_b64 s[50:51], 0

.LBB1_20:
	s_waitcnt lgkmcnt(0)
	s_barrier
	s_setprio 1
	s_waitcnt lgkmcnt(0)
	v_mfma_f32_16x16x32_f16 v[64:67], v[148:151], v[188:191], v[64:67]
	v_mfma_f32_16x16x32_f16 v[64:67], v[152:155], v[192:195], v[64:67]
	v_mfma_f32_16x16x32_f16 v[56:59], v[160:163], v[192:195], v[56:59]
	v_mfma_f32_16x16x32_f16 v[56:59], v[156:159], v[188:191], v[56:59]
	v_mfma_f32_16x16x32_f16 v[40:43], v[156:159], v[176:179], v[40:43]
	v_mfma_f32_16x16x32_f16 v[40:43], v[160:163], v[180:183], v[40:43]
	v_mfma_f32_16x16x32_f16 v[48:51], v[152:155], v[180:183], v[48:51]
	v_mfma_f32_16x16x32_f16 v[48:51], v[148:151], v[176:179], v[48:51]
	v_mfma_f32_16x16x32_f16 v[32:35], v[148:151], v[172:175], v[32:35]
	v_mfma_f32_16x16x32_f16 v[32:35], v[152:155], v[184:187], v[32:35]
	v_mfma_f32_16x16x32_f16 v[24:27], v[160:163], v[184:187], v[24:27]
	v_mfma_f32_16x16x32_f16 v[24:27], v[156:159], v[172:175], v[24:27]
	v_mfma_f32_16x16x32_f16 v[8:11], v[156:159], v[164:167], v[8:11]
	v_mfma_f32_16x16x32_f16 v[8:11], v[160:163], v[168:171], v[8:11]
	v_mfma_f32_16x16x32_f16 v[16:19], v[152:155], v[168:171], v[16:19]
	v_mfma_f32_16x16x32_f16 v[16:19], v[148:151], v[164:167], v[16:19]
	s_setprio 0
	s_setprio 1
	v_mfma_f32_16x16x32_f16 v[60:63], v[132:135], v[188:191], v[60:63]
	v_mfma_f32_16x16x32_f16 v[60:63], v[136:139], v[192:195], v[60:63]
	v_mfma_f32_16x16x32_f16 v[52:55], v[144:147], v[192:195], v[52:55]
	v_mfma_f32_16x16x32_f16 v[52:55], v[140:143], v[188:191], v[52:55]
	v_mfma_f32_16x16x32_f16 v[36:39], v[140:143], v[176:179], v[36:39]
	v_mfma_f32_16x16x32_f16 v[36:39], v[144:147], v[180:183], v[36:39]
	v_mfma_f32_16x16x32_f16 v[44:47], v[136:139], v[180:183], v[44:47]
	v_mfma_f32_16x16x32_f16 v[44:47], v[132:135], v[176:179], v[44:47]
	v_mfma_f32_16x16x32_f16 v[28:31], v[132:135], v[172:175], v[28:31]
	v_mfma_f32_16x16x32_f16 v[28:31], v[136:139], v[184:187], v[28:31]
	v_mfma_f32_16x16x32_f16 v[20:23], v[144:147], v[184:187], v[20:23]
	v_mfma_f32_16x16x32_f16 v[20:23], v[140:143], v[172:175], v[20:23]
	v_mfma_f32_16x16x32_f16 v[4:7], v[140:143], v[164:167], v[4:7]
	v_mfma_f32_16x16x32_f16 v[4:7], v[144:147], v[168:171], v[4:7]
	v_mfma_f32_16x16x32_f16 v[12:15], v[136:139], v[168:171], v[12:15]
	v_mfma_f32_16x16x32_f16 v[12:15], v[132:135], v[164:167], v[12:15]
	s_setprio 0
	s_barrier
	s_add_u32 s48, s48, 0x100000
	ds_read_b128 v[148:151], v228 offset:32768
	ds_read_b128 v[152:155], v229 offset:32768
	s_addc_u32 s49, s49, 0
	s_mov_b32 m0, s57
	ds_read_b128 v[156:159], v228 offset:34816
	ds_read_b128 v[160:163], v229 offset:34816
	ds_read_b128 v[132:135], v228 offset:49152
	ds_read_b128 v[136:139], v229 offset:49152
	ds_read_b128 v[140:143], v228 offset:51200
	ds_read_b128 v[144:147], v229 offset:51200
	ds_read_b128 v[188:191], v226 offset:32768
	ds_read_b128 v[176:179], v226 offset:34816
	ds_read_b128 v[192:195], v227 offset:32768
	ds_read_b128 v[180:183], v227 offset:34816
	ds_read_b128 v[172:175], v226 offset:36864
	ds_read_b128 v[164:167], v226 offset:38912
	ds_read_b128 v[184:187], v227 offset:36864
	ds_read_b128 v[168:171], v227 offset:38912
	global_load_lds_dwordx4 v202, s[48:49]
	s_mov_b32 m0, s58
	s_nop 0
	global_load_lds_dwordx4 v198, s[48:49]
	s_mov_b64 s[48:49], -1
	s_mov_b64 vcc, s[4:5]
	s_cbranch_vccz .LBB1_22
	s_waitcnt vmcnt(9)
	s_mov_b64 s[48:49], 0

.LBB1_24:
	s_waitcnt lgkmcnt(0)
	s_barrier
	s_setprio 1
	s_waitcnt lgkmcnt(0)
	v_mfma_f32_16x16x32_f16 v[128:131], v[148:151], v[188:191], v[128:131]
	v_mfma_f32_16x16x32_f16 v[128:131], v[152:155], v[192:195], v[128:131]
	v_mfma_f32_16x16x32_f16 v[120:123], v[160:163], v[192:195], v[120:123]
	v_mfma_f32_16x16x32_f16 v[120:123], v[156:159], v[188:191], v[120:123]
	v_mfma_f32_16x16x32_f16 v[104:107], v[156:159], v[176:179], v[104:107]
	v_mfma_f32_16x16x32_f16 v[104:107], v[160:163], v[180:183], v[104:107]
	v_mfma_f32_16x16x32_f16 v[112:115], v[152:155], v[180:183], v[112:115]
	v_mfma_f32_16x16x32_f16 v[112:115], v[148:151], v[176:179], v[112:115]
	v_mfma_f32_16x16x32_f16 v[96:99], v[148:151], v[172:175], v[96:99]
	v_mfma_f32_16x16x32_f16 v[96:99], v[152:155], v[184:187], v[96:99]
	v_mfma_f32_16x16x32_f16 v[88:91], v[160:163], v[184:187], v[88:91]
	v_mfma_f32_16x16x32_f16 v[88:91], v[156:159], v[172:175], v[88:91]
	v_mfma_f32_16x16x32_f16 v[72:75], v[156:159], v[164:167], v[72:75]
	v_mfma_f32_16x16x32_f16 v[72:75], v[160:163], v[168:171], v[72:75]
	v_mfma_f32_16x16x32_f16 v[80:83], v[152:155], v[168:171], v[80:83]
	v_mfma_f32_16x16x32_f16 v[80:83], v[148:151], v[164:167], v[80:83]
	s_setprio 0
	s_setprio 1
	v_mfma_f32_16x16x32_f16 v[124:127], v[132:135], v[188:191], v[124:127]
	v_mfma_f32_16x16x32_f16 v[124:127], v[136:139], v[192:195], v[124:127]
	v_mfma_f32_16x16x32_f16 v[116:119], v[144:147], v[192:195], v[116:119]
	v_mfma_f32_16x16x32_f16 v[116:119], v[140:143], v[188:191], v[116:119]
	v_mfma_f32_16x16x32_f16 v[100:103], v[140:143], v[176:179], v[100:103]
	v_mfma_f32_16x16x32_f16 v[100:103], v[144:147], v[180:183], v[100:103]
	v_mfma_f32_16x16x32_f16 v[108:111], v[136:139], v[180:183], v[108:111]
	v_mfma_f32_16x16x32_f16 v[108:111], v[132:135], v[176:179], v[108:111]
	v_mfma_f32_16x16x32_f16 v[92:95], v[132:135], v[172:175], v[92:95]
	v_mfma_f32_16x16x32_f16 v[92:95], v[136:139], v[184:187], v[92:95]
	v_mfma_f32_16x16x32_f16 v[84:87], v[144:147], v[184:187], v[84:87]
	v_mfma_f32_16x16x32_f16 v[84:87], v[140:143], v[172:175], v[84:87]
	v_mfma_f32_16x16x32_f16 v[68:71], v[140:143], v[164:167], v[68:71]
	v_mfma_f32_16x16x32_f16 v[68:71], v[144:147], v[168:171], v[68:71]
	v_mfma_f32_16x16x32_f16 v[76:79], v[136:139], v[168:171], v[76:79]
	v_mfma_f32_16x16x32_f16 v[76:79], v[132:135], v[164:167], v[76:79]
	s_setprio 0
	s_barrier
	s_mov_b32 m0, s59
	s_add_u32 s4, s46, 0x100080
	ds_read_b128 v[164:167], v226 offset:49152
	ds_read_b128 v[168:171], v226 offset:51200
	ds_read_b128 v[172:175], v227 offset:49152
	ds_read_b128 v[176:179], v227 offset:51200
	ds_read_b128 v[180:183], v226 offset:53248
	ds_read_b128 v[184:187], v226 offset:55296
	ds_read_b128 v[188:191], v227 offset:53248
	ds_read_b128 v[192:195], v227 offset:55296
	global_load_lds_dwordx4 v200, s[84:85]
	s_mov_b32 m0, s60
	s_addc_u32 s5, s47, 0
	global_load_lds_dwordx4 v196, s[84:85]
	s_mov_b32 m0, s63
	s_nop 0
	global_load_lds_dwordx4 v200, s[4:5]
	s_mov_b32 m0, s64
	s_nop 0
	global_load_lds_dwordx4 v196, s[4:5]
	s_mov_b32 m0, s61
	s_nop 0
	global_load_lds_dwordx4 v202, s[86:87]
	s_mov_b32 m0, s62
	s_nop 0
	global_load_lds_dwordx4 v198, s[86:87]
	s_cmp_lg_u32 s83, 0
	s_cbranch_scc0 .Lk1_p4w8
	s_waitcnt vmcnt(9)
	s_branch .Lk1_p4we

.Lk1_p4we:
	s_waitcnt lgkmcnt(0)
	s_barrier
	s_setprio 1
	s_waitcnt lgkmcnt(0)
	v_mfma_f32_16x16x32_f16 v[64:67], v[148:151], v[164:167], v[64:67]
	v_mfma_f32_16x16x32_f16 v[64:67], v[152:155], v[172:175], v[64:67]
	v_mfma_f32_16x16x32_f16 v[56:59], v[160:163], v[172:175], v[56:59]
	v_mfma_f32_16x16x32_f16 v[56:59], v[156:159], v[164:167], v[56:59]
	v_mfma_f32_16x16x32_f16 v[40:43], v[156:159], v[168:171], v[40:43]
	v_mfma_f32_16x16x32_f16 v[40:43], v[160:163], v[176:179], v[40:43]
	v_mfma_f32_16x16x32_f16 v[48:51], v[152:155], v[176:179], v[48:51]
	v_mfma_f32_16x16x32_f16 v[48:51], v[148:151], v[168:171], v[48:51]
	v_mfma_f32_16x16x32_f16 v[32:35], v[148:151], v[180:183], v[32:35]
	v_mfma_f32_16x16x32_f16 v[32:35], v[152:155], v[188:191], v[32:35]
	v_mfma_f32_16x16x32_f16 v[24:27], v[160:163], v[188:191], v[24:27]
	v_mfma_f32_16x16x32_f16 v[24:27], v[156:159], v[180:183], v[24:27]
	v_mfma_f32_16x16x32_f16 v[8:11], v[156:159], v[184:187], v[8:11]
	v_mfma_f32_16x16x32_f16 v[8:11], v[160:163], v[192:195], v[8:11]
	v_mfma_f32_16x16x32_f16 v[16:19], v[152:155], v[192:195], v[16:19]
	v_mfma_f32_16x16x32_f16 v[16:19], v[148:151], v[184:187], v[16:19]
	s_setprio 0
	s_setprio 1
	v_mfma_f32_16x16x32_f16 v[60:63], v[132:135], v[164:167], v[60:63]
	v_mfma_f32_16x16x32_f16 v[60:63], v[136:139], v[172:175], v[60:63]
	v_mfma_f32_16x16x32_f16 v[52:55], v[144:147], v[172:175], v[52:55]
	v_mfma_f32_16x16x32_f16 v[52:55], v[140:143], v[164:167], v[52:55]
	v_mfma_f32_16x16x32_f16 v[36:39], v[140:143], v[168:171], v[36:39]
	v_mfma_f32_16x16x32_f16 v[36:39], v[144:147], v[176:179], v[36:39]
	v_mfma_f32_16x16x32_f16 v[44:47], v[136:139], v[176:179], v[44:47]
	v_mfma_f32_16x16x32_f16 v[44:47], v[132:135], v[168:171], v[44:47]
	v_mfma_f32_16x16x32_f16 v[28:31], v[132:135], v[180:183], v[28:31]
	v_mfma_f32_16x16x32_f16 v[28:31], v[136:139], v[188:191], v[28:31]
	v_mfma_f32_16x16x32_f16 v[20:23], v[144:147], v[188:191], v[20:23]
	v_mfma_f32_16x16x32_f16 v[20:23], v[140:143], v[180:183], v[20:23]
	v_mfma_f32_16x16x32_f16 v[4:7], v[140:143], v[184:187], v[4:7]
	v_mfma_f32_16x16x32_f16 v[4:7], v[144:147], v[192:195], v[4:7]
	v_mfma_f32_16x16x32_f16 v[12:15], v[136:139], v[192:195], v[12:15]
	v_mfma_f32_16x16x32_f16 v[12:15], v[132:135], v[184:187], v[12:15]
	s_setprio 0
	s_barrier
	s_add_u32 s80, s80, 0x100
	s_addc_u32 s81, s81, 0
	s_add_u32 s44, s44, 0x100
	s_addc_u32 s45, s45, 0
	s_cmp_gt_u32 s82, 61
	s_cbranch_scc1 .LBB1_4
	s_mov_b32 s48, s82
	s_branch .LBB1_9

.LBB1_30:
	s_endpgm
	s_nop 0
	s_nop 0
	s_nop 0
	s_nop 0
	s_nop 0
	s_nop 0
	s_nop 0
	s_nop 0
	s_nop 0
	s_nop 0
	s_nop 0
	s_nop 0
	s_nop 0
	s_nop 0
	s_nop 0
	s_nop 0
	s_nop 0
	s_nop 0
	s_nop 0
	s_nop 0
	s_nop 0
	s_nop 0
	s_nop 0
	s_nop 0
	s_nop 0
	s_nop 0
	s_nop 0
	s_nop 0
	s_nop 0
	s_nop 0
	s_nop 0
	s_nop 0
	s_nop 0
	s_nop 0
	s_nop 0
	s_nop 0
	s_nop 0
	s_nop 0
	s_nop 0
	s_nop 0
	s_nop 0
	s_nop 0
	s_nop 0
	s_nop 0
	s_nop 0
	s_nop 0
	s_nop 0
	s_endpgm
